# speedup vs baseline: 1.0114x; 1.0061x over previous
_Z4ln_kPKfS0_S0_S0_PfPDF16_:
	v_lshlrev_b32_e32 v59, 4, v0
	s_getpc_b64 s[14:15]
	s_add_u32 s14, s14, 0xa2f8
	s_addc_u32 s15, s15, 0x0
	global_load_dword v60, v59, s[14:15]
	v_add_u32_e32 v59, 0x1000, v59
	global_load_dword v60, v59, s[14:15]
	v_add_u32_e32 v59, 0x1000, v59
	global_load_dword v60, v59, s[14:15]
	v_add_u32_e32 v59, 0x1000, v59
	global_load_dword v60, v59, s[14:15]
	v_lshlrev_b32_e32 v59, 4, v0
	s_load_dwordx8 s[4:11], s[0:1], 0x0
	v_lshrrev_b32_e32 v1, 6, v0
	v_lshl_or_b32 v54, s2, 2, v1
	s_movk_i32 s12, 0xc00
	v_and_b32_e32 v55, 63, v0
	s_waitcnt lgkmcnt(0)
	v_mov_b64_e32 v[2:3], s[4:5]
	v_mad_i64_i32 v[4:5], s[2:3], v54, s12, v[2:3]
	v_mov_b64_e32 v[2:3], s[6:7]
	v_mad_i64_i32 v[6:7], s[2:3], v54, s12, v[2:3]
	v_lshlrev_b32_e32 v2, 4, v55
	v_mov_b32_e32 v3, 0
	v_lshl_add_u64 v[30:31], v[6:7], 0, v[2:3]
	v_lshl_add_u64 v[28:29], v[4:5], 0, v[2:3]
	global_load_dwordx4 v[4:7], v[30:31], off
	global_load_dwordx4 v[8:11], v[28:29], off
	global_load_dwordx4 v[12:15], v[28:29], off offset:1024
	global_load_dwordx4 v[16:19], v[30:31], off offset:1024
	global_load_dwordx4 v[20:23], v[28:29], off offset:2048
	global_load_dwordx4 v[24:27], v[30:31], off offset:2048
	s_nop 0
	global_load_dwordx4 v[28:31], v2, s[8:9]
	global_load_dwordx4 v[32:35], v2, s[10:11]
	global_load_dwordx4 v[36:39], v2, s[8:9] offset:1024
	global_load_dwordx4 v[40:43], v2, s[10:11] offset:1024
	s_load_dwordx4 s[4:7], s[0:1], 0x20
	v_and_b32_e32 v50, 16, v0
	v_cmp_eq_u32_e32 vcc, 0, v50
	v_and_b32_e32 v51, 32, v0
	v_mov_b32_e32 v56, 0x2b8cbccc
	s_waitcnt lgkmcnt(0)
	v_mov_b64_e32 v[0:1], s[4:5]
	v_mad_i64_i32 v[0:1], s[0:1], v54, s12, v[0:1]
	v_cmp_eq_u32_e64 s[0:1], 0, v51
	s_mov_b32 s3, 0xf800000
	s_movk_i32 s2, 0x680
	v_mov_b64_e32 v[44:45], s[6:7]
	v_mov_b32_e32 v57, 0x260
	s_waitcnt vmcnt(8)
	v_pk_add_f32 v[46:47], v[8:9], v[4:5]
	v_pk_add_f32 v[48:49], v[10:11], v[6:7]
	global_load_dwordx4 v[4:7], v2, s[8:9] offset:2048
	global_load_dwordx4 v[8:11], v2, s[10:11] offset:2048
	s_waitcnt vmcnt(8)
	v_pk_add_f32 v[12:13], v[12:13], v[16:17]
	s_waitcnt vmcnt(6)
	v_pk_add_f32 v[16:17], v[20:21], v[24:25]
	v_pk_add_f32 v[14:15], v[14:15], v[18:19]
	v_pk_add_f32 v[18:19], v[22:23], v[26:27]
	v_add_f32_e32 v52, v46, v47
	v_mov_b32_e32 v20, v12
	v_mov_b32_e32 v21, v16
	v_mov_b32_e32 v22, v13
	v_mov_b32_e32 v23, v17
	v_mov_b32_e32 v24, v14
	v_mov_b32_e32 v25, v18
	v_add_f32_e32 v52, v52, v48
	v_pk_add_f32 v[20:21], v[20:21], v[22:23]
	v_mov_b32_e32 v26, v15
	v_mov_b32_e32 v27, v19
	v_add_f32_e32 v22, v52, v49
	v_pk_add_f32 v[20:21], v[20:21], v[24:25]
	v_add_f32_e32 v22, 0, v22
	v_pk_add_f32 v[20:21], v[20:21], v[26:27]
	s_nop 0
	v_add_f32_e32 v20, v22, v20
	v_add_f32_e32 v20, v20, v21
	s_nop 1
	v_add_f32_dpp v20, v20, v20 quad_perm:[1,0,3,2] row_mask:0xf bank_mask:0xf bound_ctrl:1
	s_nop 1
	v_add_f32_dpp v20, v20, v20 quad_perm:[2,3,0,1] row_mask:0xf bank_mask:0xf bound_ctrl:1
	s_nop 1
	v_add_f32_dpp v20, v20, v20 row_half_mirror row_mask:0xf bank_mask:0xf bound_ctrl:1
	s_nop 1
	v_add_f32_dpp v20, v20, v20 row_mirror row_mask:0xf bank_mask:0xf bound_ctrl:1
	v_mov_b32_e32 v21, v20
	v_mov_b32_e32 v22, v20
	s_nop 1
	v_permlane16_swap_b32_e32 v21, v22
	v_cndmask_b32_e32 v21, v21, v22, vcc
	v_add_f32_e32 v20, v20, v21
	v_mov_b32_e32 v21, v20
	v_mov_b32_e32 v22, v20
	s_nop 1
	v_permlane32_swap_b32_e32 v21, v22
	v_cndmask_b32_e64 v21, v21, v22, s[0:1]
	v_add_f32_e32 v20, v20, v21
	v_mul_f32_e32 v20, 0x3aaaaaab, v20
	v_pk_add_f32 v[22:23], v[46:47], v[20:21] op_sel_hi:[1,0] neg_lo:[0,1] neg_hi:[0,1]
	v_pk_add_f32 v[16:17], v[16:17], v[20:21] op_sel_hi:[1,0] neg_lo:[0,1] neg_hi:[0,1]
	v_pk_add_f32 v[24:25], v[48:49], v[20:21] op_sel_hi:[1,0] neg_lo:[0,1] neg_hi:[0,1]
	v_pk_add_f32 v[12:13], v[12:13], v[20:21] op_sel_hi:[1,0] neg_lo:[0,1] neg_hi:[0,1]
	v_mov_b32_e32 v48, v17
	v_mov_b32_e32 v49, v23
	v_pk_add_f32 v[14:15], v[14:15], v[20:21] op_sel_hi:[1,0] neg_lo:[0,1] neg_hi:[0,1]
	v_pk_add_f32 v[18:19], v[18:19], v[20:21] op_sel_hi:[1,0] neg_lo:[0,1] neg_hi:[0,1]
	v_pk_mul_f32 v[20:21], v[12:13], v[12:13]
	v_mov_b32_e32 v46, v16
	v_mov_b32_e32 v47, v22
	v_pk_mul_f32 v[48:49], v[48:49], v[48:49]
	v_pk_mul_f32 v[26:27], v[14:15], v[14:15]
	v_mov_b32_e32 v50, v18
	v_mov_b32_e32 v51, v24
	v_add_f32_e32 v58, v20, v21
	v_pk_fma_f32 v[20:21], v[46:47], v[46:47], v[48:49]
	v_mov_b32_e32 v52, v19
	v_mov_b32_e32 v53, v25
	v_add_f32_e32 v26, v26, v58
	v_pk_fma_f32 v[20:21], v[50:51], v[50:51], v[20:21]
	v_add_f32_e32 v26, v27, v26
	v_pk_fma_f32 v[20:21], v[52:53], v[52:53], v[20:21]
	s_nop 0
	v_add_f32_e32 v21, v21, v26
	v_add_f32_e32 v20, v20, v21
	s_nop 1
	v_add_f32_dpp v20, v20, v20 quad_perm:[1,0,3,2] row_mask:0xf bank_mask:0xf bound_ctrl:1
	s_nop 1
	v_add_f32_dpp v20, v20, v20 quad_perm:[2,3,0,1] row_mask:0xf bank_mask:0xf bound_ctrl:1
	s_nop 1
	v_add_f32_dpp v20, v20, v20 row_half_mirror row_mask:0xf bank_mask:0xf bound_ctrl:1
	s_nop 1
	v_add_f32_dpp v20, v20, v20 row_mirror row_mask:0xf bank_mask:0xf bound_ctrl:1
	v_mov_b32_e32 v21, v20
	v_mov_b32_e32 v26, v20
	s_nop 1
	v_permlane16_swap_b32_e32 v21, v26
	v_cndmask_b32_e32 v21, v21, v26, vcc
	v_add_f32_e32 v20, v20, v21
	v_mov_b32_e32 v21, v20
	v_mov_b32_e32 v26, v20
	s_nop 1
	v_permlane32_swap_b32_e32 v21, v26
	v_cndmask_b32_e64 v21, v21, v26, s[0:1]
	v_add_f32_e32 v20, v20, v21
	v_fmac_f32_e32 v56, 0x3aaaaaab, v20
	v_mul_f32_e32 v20, 0x4f800000, v56
	v_cmp_gt_f32_e32 vcc, s3, v56
	v_lshl_add_u64 v[26:27], v[0:1], 0, v[2:3]
	s_nop 0
	v_cndmask_b32_e32 v46, v56, v20, vcc
	v_sqrt_f32_e32 v47, v46
	v_mad_i64_i32 v[20:21], s[0:1], v54, s2, v[44:45]
	v_add_u32_e32 v0, -1, v47
	v_add_u32_e32 v1, 1, v47
	v_fma_f32 v2, -v0, v47, v46
	v_fma_f32 v44, -v1, v47, v46
	v_cmp_ge_f32_e64 s[0:1], 0, v2
	v_lshlrev_b32_e32 v2, 3, v55
	v_lshl_add_u64 v[20:21], v[20:21], 0, v[2:3]
	v_cndmask_b32_e64 v0, v47, v0, s[0:1]
	v_cmp_lt_f32_e64 s[0:1], 0, v44
	s_nop 1
	v_cndmask_b32_e64 v0, v0, v1, s[0:1]
	v_mul_f32_e32 v1, 0x37800000, v0
	v_cndmask_b32_e32 v0, v0, v1, vcc
	v_cmp_class_f32_e32 vcc, v46, v57
	s_nop 1
	v_cndmask_b32_e32 v0, v0, v46, vcc
	v_div_scale_f32 v1, s[0:1], v0, v0, 1.0
	v_rcp_f32_e32 v44, v1
	s_nop 0
	v_fma_f32 v2, -v1, v44, 1.0
	v_fmac_f32_e32 v44, v2, v44
	v_div_scale_f32 v2, vcc, 1.0, v0, 1.0
	v_mul_f32_e32 v3, v2, v44
	v_fma_f32 v45, -v1, v3, v2
	v_fmac_f32_e32 v3, v45, v44
	v_fma_f32 v1, -v1, v3, v2
	v_div_fmas_f32 v1, v1, v44, v3
	v_div_fixup_f32 v44, v1, v0, 1.0
	v_pk_mul_f32 v[0:1], v[22:23], v[44:45] op_sel_hi:[1,0]
	v_pk_mul_f32 v[2:3], v[24:25], v[44:45] op_sel_hi:[1,0]
	v_pk_mul_f32 v[12:13], v[12:13], v[44:45] op_sel_hi:[1,0]
	v_pk_mul_f32 v[14:15], v[14:15], v[44:45] op_sel_hi:[1,0]
	v_pk_mul_f32 v[16:17], v[16:17], v[44:45] op_sel_hi:[1,0]
	s_waitcnt vmcnt(4)
	v_pk_fma_f32 v[0:1], v[28:29], v[0:1], v[32:33]
	v_pk_fma_f32 v[2:3], v[30:31], v[2:3], v[34:35]
	s_waitcnt vmcnt(2)
	v_pk_fma_f32 v[12:13], v[12:13], v[36:37], v[40:41]
	v_pk_fma_f32 v[14:15], v[14:15], v[38:39], v[42:43]
	s_waitcnt vmcnt(0)
	v_pk_fma_f32 v[4:5], v[16:17], v[4:5], v[8:9]
	v_pk_mul_f32 v[8:9], v[18:19], v[44:45] op_sel_hi:[1,0]
	global_store_dwordx4 v[26:27], v[0:3], off
	v_pk_fma_f32 v[6:7], v[8:9], v[6:7], v[10:11]
	s_nop 0
	v_cvt_pk_f16_f32 v3, v2, v3
	v_cvt_pk_f16_f32 v2, v0, v1
	v_cvt_pk_f16_f32 v1, v14, v15
	v_cvt_pk_f16_f32 v0, v12, v13
	global_store_dwordx2 v[20:21], v[2:3], off
	global_store_dwordx4 v[26:27], v[12:15], off offset:1024
	global_store_dwordx2 v[20:21], v[0:1], off offset:512
	global_store_dwordx4 v[26:27], v[4:7], off offset:2048
	v_cvt_pk_f16_f32 v1, v6, v7
	v_cvt_pk_f16_f32 v0, v4, v5
	global_store_dwordx2 v[20:21], v[0:1], off offset:1024
	s_endpgm
